# DSA indexer: f16 order-key sign mask built with v_bfe_i32/v_or instead of v_cmp + s_nop + v_cndmask (17 sites), on top of v056
# baseline (speedup 1.0000x reference)
.LBB0_1047:
	s_add_i32 s8, s4, 16
	s_min_i32 s6, s8, s29
	s_lshl_b32 s6, s6, 5
	v_mad_i64_i32 v[40:41], s[6:7], s6, v235, v[14:15]
	global_load_dwordx4 v[176:179], v[40:41], off
	global_load_dwordx4 v[172:175], v[40:41], off offset:32
	global_load_dwordx4 v[168:171], v[40:41], off offset:64
	global_load_dwordx4 v[164:167], v[40:41], off offset:96
	ds_read_b128 v[56:59], v203
	ds_read_b128 v[64:67], v203 offset:1024
	s_waitcnt vmcnt(15)
	v_mfma_f32_32x32x16_bf16 v[40:55], v[160:163], v[96:99], 0
	v_cvt_f16_f32_e32 v0, v32
	v_bfe_i32 v32, v0, 15, 1
	v_or_b32_e32 v32, 0x8000, v32
	v_xor_b32_e32 v32, v32, v0
	v_add_u32_e32 v0, 0xfffe9c40, v190
	v_lshl_add_u64 v[60:61], v[0:1], 1, s[12:13]
	v_lshrrev_b32_e32 v0, 4, v32
	v_and_b32_e32 v0, 0xffc, v0
	global_store_short v[60:61], v32, off
	v_add_u32_e32 v0, v187, v0
	ds_add_u32 v0, v228 offset:17408
	s_waitcnt vmcnt(15)
	v_mfma_f32_32x32x16_bf16 v[40:55], v[156:159], v[10:13], v[40:55]
	s_waitcnt vmcnt(14)
	v_mfma_f32_32x32x16_bf16 v[40:55], v[152:155], v[6:9], v[40:55]
	v_cvt_f16_f32_e32 v0, v33
	v_bfe_i32 v32, v0, 15, 1
	v_or_b32_e32 v32, 0x8000, v32
	v_xor_b32_e32 v60, v32, v0
	v_add_u32_e32 v0, 0xfffebc80, v190
	v_lshl_add_u64 v[32:33], v[0:1], 1, s[12:13]
	v_lshrrev_b32_e32 v0, 4, v60
	v_and_b32_e32 v0, 0xffc, v0
	global_store_short v[32:33], v60, off
	v_add_u32_e32 v0, v187, v0
	ds_add_u32 v0, v228 offset:21504
	s_waitcnt vmcnt(14)
	v_mfma_f32_32x32x16_bf16 v[40:55], v[148:151], v[2:5], v[40:55]
	v_mfma_f32_32x32x16_bf16 v[80:95], v[144:147], v[96:99], 0
	v_cvt_f16_f32_e32 v0, v34
	v_bfe_i32 v32, v0, 15, 1
	v_or_b32_e32 v32, 0x8000, v32
	v_xor_b32_e32 v34, v32, v0
	v_add_u32_e32 v0, 0xfffedcc0, v190
	v_lshl_add_u64 v[32:33], v[0:1], 1, s[12:13]
	v_lshrrev_b32_e32 v0, 4, v34
	v_and_b32_e32 v0, 0xffc, v0
	global_store_short v[32:33], v34, off
	v_add_u32_e32 v0, v187, v0
	ds_add_u32 v0, v228 offset:25600
	v_mfma_f32_32x32x16_bf16 v[80:95], v[140:143], v[10:13], v[80:95]
	v_cvt_pk_bf16_f32 v0, v40, v41
	v_pk_max_i16 v40, v0, 0
	v_cvt_pk_bf16_f32 v0, v42, v43
	v_pk_max_i16 v41, v0, 0
	v_cvt_pk_bf16_f32 v0, v44, v45
	v_pk_max_i16 v42, v0, 0
	v_cvt_pk_bf16_f32 v0, v46, v47
	v_pk_max_i16 v43, v0, 0
	v_mfma_f32_32x32x16_bf16 v[80:95], v[136:139], v[6:9], v[80:95]
	ds_read_b128 v[204:207], v203 offset:2048
	ds_read_b128 v[240:243], v203 offset:3072
	v_cvt_pk_bf16_f32 v0, v48, v49
	v_pk_max_i16 v44, v0, 0
	v_cvt_pk_bf16_f32 v0, v50, v51
	v_pk_max_i16 v45, v0, 0
	v_cvt_pk_bf16_f32 v0, v52, v53
	v_pk_max_i16 v46, v0, 0
	v_cvt_pk_bf16_f32 v0, v54, v55
	v_pk_max_i16 v47, v0, 0
	v_mfma_f32_32x32x16_bf16 v[80:95], v[132:135], v[2:5], v[80:95]
	v_cvt_f16_f32_e32 v0, v35
	v_bfe_i32 v32, v0, 15, 1
	v_or_b32_e32 v32, 0x8000, v32
	v_xor_b32_e32 v34, v32, v0
	v_add_u32_e32 v0, 0xfffefd00, v190
	v_lshl_add_u64 v[32:33], v[0:1], 1, s[12:13]
	v_lshrrev_b32_e32 v0, 4, v34
	v_and_b32_e32 v0, 0xffc, v0
	global_store_short v[32:33], v34, off
	v_add_u32_e32 v0, v187, v0
	ds_add_u32 v0, v228 offset:29696
	s_waitcnt lgkmcnt(7)
	v_mfma_f32_32x32x16_bf16 v[48:63], v[56:59], v[40:43], 0
	s_waitcnt lgkmcnt(6)
	v_mfma_f32_32x32x16_bf16 v[48:63], v[64:67], v[44:47], v[48:63]
	v_mfma_f32_32x32x16_bf16 v[64:79], v[128:131], v[96:99], 0
	v_cvt_f16_f32_e32 v0, v36
	v_bfe_i32 v32, v0, 15, 1
	v_or_b32_e32 v32, 0x8000, v32
	v_xor_b32_e32 v34, v32, v0
	v_add_u32_e32 v0, 0xffff9e40, v190
	v_lshl_add_u64 v[32:33], v[0:1], 1, s[12:13]
	v_lshrrev_b32_e32 v0, 4, v34
	v_and_b32_e32 v0, 0xffc, v0
	global_store_short v[32:33], v34, off
	v_add_u32_e32 v0, v187, v0
	ds_add_u32 v0, v228 offset:50176
	v_mfma_f32_32x32x16_bf16 v[64:79], v[124:127], v[10:13], v[64:79]
	v_cvt_pk_bf16_f32 v0, v80, v81
	v_pk_max_i16 v32, v0, 0
	v_cvt_pk_bf16_f32 v0, v82, v83
	v_pk_max_i16 v33, v0, 0
	v_cvt_pk_bf16_f32 v0, v84, v85
	v_pk_max_i16 v34, v0, 0
	v_cvt_pk_bf16_f32 v0, v86, v87
	v_pk_max_i16 v35, v0, 0
	v_mfma_f32_32x32x16_bf16 v[64:79], v[120:123], v[6:9], v[64:79]
	ds_read_b128 v[44:47], v203 offset:4096
	ds_read_b128 v[216:219], v203 offset:5120
	v_cvt_pk_bf16_f32 v0, v88, v89
	v_pk_max_i16 v40, v0, 0
	v_cvt_pk_bf16_f32 v0, v90, v91
	v_pk_max_i16 v41, v0, 0
	v_cvt_pk_bf16_f32 v0, v92, v93
	v_pk_max_i16 v42, v0, 0
	v_cvt_pk_bf16_f32 v0, v94, v95
	v_pk_max_i16 v43, v0, 0
	v_mfma_f32_32x32x16_bf16 v[64:79], v[116:119], v[2:5], v[64:79]
	s_waitcnt lgkmcnt(5)
	v_mfma_f32_32x32x16_bf16 v[48:63], v[204:207], v[32:35], v[48:63]
	v_cvt_f16_f32_e32 v0, v37
	v_bfe_i32 v32, v0, 15, 1
	v_or_b32_e32 v32, 0x8000, v32
	v_xor_b32_e32 v34, v32, v0
	v_add_u32_e32 v0, 0xffffbe80, v190
	v_lshl_add_u64 v[32:33], v[0:1], 1, s[12:13]
	v_lshrrev_b32_e32 v0, 4, v34
	v_and_b32_e32 v0, 0xffc, v0
	global_store_short v[32:33], v34, off
	v_add_u32_e32 v0, v187, v0
	ds_add_u32 v0, v228 offset:54272
	s_waitcnt lgkmcnt(5)
	v_mfma_f32_32x32x16_bf16 v[48:63], v[240:243], v[40:43], v[48:63]
	v_mfma_f32_32x32x16_bf16 v[80:95], v[112:115], v[96:99], 0
	v_cvt_f16_f32_e32 v0, v38
	v_bfe_i32 v32, v0, 15, 1
	v_or_b32_e32 v32, 0x8000, v32
	v_xor_b32_e32 v34, v32, v0
	v_add_u32_e32 v0, 0xffffdec0, v190
	v_lshl_add_u64 v[32:33], v[0:1], 1, s[12:13]
	v_lshrrev_b32_e32 v0, 4, v34
	v_and_b32_e32 v0, 0xffc, v0
	global_store_short v[32:33], v34, off
	v_add_u32_e32 v0, v187, v0
	ds_add_u32 v0, v228 offset:58368
	v_mfma_f32_32x32x16_bf16 v[80:95], v[108:111], v[10:13], v[80:95]
	v_cvt_pk_bf16_f32 v0, v64, v65
	v_pk_max_i16 v10, v0, 0
	v_cvt_pk_bf16_f32 v0, v66, v67
	v_pk_max_i16 v11, v0, 0
	v_cvt_pk_bf16_f32 v0, v68, v69
	v_pk_max_i16 v12, v0, 0
	v_cvt_pk_bf16_f32 v0, v70, v71
	v_pk_max_i16 v13, v0, 0
	v_mfma_f32_32x32x16_bf16 v[80:95], v[104:107], v[6:9], v[80:95]
	v_cvt_pk_bf16_f32 v0, v72, v73
	ds_read_b128 v[32:35], v203 offset:6144
	ds_read_b128 v[40:43], v203 offset:7168
	v_pk_max_i16 v6, v0, 0
	v_cvt_pk_bf16_f32 v0, v74, v75
	v_pk_max_i16 v7, v0, 0
	v_cvt_pk_bf16_f32 v0, v76, v77
	v_pk_max_i16 v8, v0, 0
	v_cvt_pk_bf16_f32 v0, v78, v79
	v_pk_max_i16 v9, v0, 0
	v_mfma_f32_32x32x16_bf16 v[80:95], v[100:103], v[2:5], v[80:95]
	v_cvt_f16_f32_e32 v0, v39
	v_bfe_i32 v2, v0, 15, 1
	v_or_b32_e32 v2, 0x8000, v2
	v_xor_b32_e32 v4, v2, v0
	v_add_u32_e32 v0, 0xffffff00, v190
	v_lshl_add_u64 v[2:3], v[0:1], 1, s[12:13]
	v_lshrrev_b32_e32 v0, 4, v4
	v_and_b32_e32 v0, 0xffc, v0
	global_store_short v[2:3], v4, off
	v_add_u32_e32 v0, v187, v0
	ds_add_u32 v0, v228 offset:62464
	s_waitcnt lgkmcnt(6)
	v_mfma_f32_32x32x16_bf16 v[48:63], v[44:47], v[10:13], v[48:63]
	s_waitcnt lgkmcnt(5)
	v_mfma_f32_32x32x16_bf16 v[48:63], v[216:219], v[6:9], v[48:63]
	v_cvt_pk_bf16_f32 v0, v80, v81
	v_pk_max_i16 v2, v0, 0
	v_cvt_pk_bf16_f32 v0, v82, v83
	v_pk_max_i16 v3, v0, 0
	v_cvt_pk_bf16_f32 v0, v84, v85
	v_pk_max_i16 v4, v0, 0
	v_cvt_pk_bf16_f32 v0, v86, v87
	v_pk_max_i16 v5, v0, 0
	v_cvt_pk_bf16_f32 v0, v88, v89
	v_pk_max_i16 v6, v0, 0
	v_cvt_pk_bf16_f32 v0, v90, v91
	v_pk_max_i16 v7, v0, 0
	v_cvt_pk_bf16_f32 v0, v92, v93
	v_pk_max_i16 v8, v0, 0
	v_cvt_pk_bf16_f32 v0, v94, v95
	v_pk_max_i16 v9, v0, 0
	s_waitcnt lgkmcnt(2)
	v_mfma_f32_32x32x16_bf16 v[48:63], v[32:35], v[2:5], v[48:63]
	s_waitcnt lgkmcnt(1)
	v_mfma_f32_32x32x16_bf16 v[48:63], v[40:43], v[6:9], v[48:63]
	s_mov_b64 s[6:7], -1
	s_cmp_ge_i32 s8, s28
	s_mov_b64 s[26:27], -1
	s_cbranch_scc1 .LBB0_1049
	s_add_i32 s6, s4, 24
	s_min_i32 s6, s6, s29
	s_lshl_b32 s6, s6, 5
	v_mad_i64_i32 v[2:3], s[6:7], s6, v235, v[14:15]
	global_load_dwordx4 v[96:99], v[2:3], off
	global_load_dwordx4 v[10:13], v[2:3], off offset:32
	global_load_dwordx4 v[6:9], v[2:3], off offset:64
	s_nop 0
	global_load_dwordx4 v[2:5], v[2:3], off offset:96
	ds_read_b128 v[56:59], v203
	ds_read_b128 v[60:63], v203 offset:1024
	s_waitcnt vmcnt(15)
	v_mfma_f32_32x32x16_bf16 v[32:47], v[160:163], v[176:179], 0
	v_cvt_f16_f32_e32 v0, v48
	v_bfe_i32 v64, v0, 15, 1
	v_or_b32_e32 v64, 0x8000, v64
	v_xor_b32_e32 v66, v64, v0
	v_add_u32_e32 v0, 0xfffe9d40, v190
	v_lshl_add_u64 v[64:65], v[0:1], 1, s[12:13]
	v_lshrrev_b32_e32 v0, 4, v66
	v_and_b32_e32 v0, 0xffc, v0
	global_store_short v[64:65], v66, off
	v_add_u32_e32 v0, v187, v0
	ds_add_u32 v0, v228 offset:17408
	s_waitcnt vmcnt(15)
	v_mfma_f32_32x32x16_bf16 v[32:47], v[156:159], v[172:175], v[32:47]
	s_waitcnt vmcnt(14)
	v_mfma_f32_32x32x16_bf16 v[32:47], v[152:155], v[168:171], v[32:47]
	v_cvt_f16_f32_e32 v0, v49
	v_bfe_i32 v64, v0, 15, 1
	v_or_b32_e32 v64, 0x8000, v64
	v_xor_b32_e32 v66, v64, v0
	v_add_u32_e32 v0, 0xfffebd80, v190
	v_lshl_add_u64 v[64:65], v[0:1], 1, s[12:13]
	v_lshrrev_b32_e32 v0, 4, v66
	v_and_b32_e32 v0, 0xffc, v0
	global_store_short v[64:65], v66, off
	v_add_u32_e32 v0, v187, v0
	ds_add_u32 v0, v228 offset:21504
	s_waitcnt vmcnt(14)
	v_mfma_f32_32x32x16_bf16 v[32:47], v[148:151], v[164:167], v[32:47]
	v_mfma_f32_32x32x16_bf16 v[72:87], v[144:147], v[176:179], 0
	v_cvt_f16_f32_e32 v0, v50
	v_bfe_i32 v64, v0, 15, 1
	v_or_b32_e32 v64, 0x8000, v64
	v_xor_b32_e32 v66, v64, v0
	v_add_u32_e32 v0, 0xfffeddc0, v190
	v_lshl_add_u64 v[64:65], v[0:1], 1, s[12:13]
	v_lshrrev_b32_e32 v0, 4, v66
	v_and_b32_e32 v0, 0xffc, v0
	global_store_short v[64:65], v66, off
	v_add_u32_e32 v0, v187, v0
	ds_add_u32 v0, v228 offset:25600
	v_mfma_f32_32x32x16_bf16 v[72:87], v[140:143], v[172:175], v[72:87]
	v_cvt_pk_bf16_f32 v0, v32, v33
	v_pk_max_i16 v32, v0, 0
	v_cvt_pk_bf16_f32 v0, v34, v35
	v_pk_max_i16 v33, v0, 0
	v_cvt_pk_bf16_f32 v0, v36, v37
	v_pk_max_i16 v34, v0, 0
	v_cvt_pk_bf16_f32 v0, v38, v39
	v_pk_max_i16 v35, v0, 0
	v_mfma_f32_32x32x16_bf16 v[72:87], v[136:139], v[168:171], v[72:87]
	ds_read_b128 v[88:91], v203 offset:2048
	ds_read_b128 v[92:95], v203 offset:3072
	v_cvt_pk_bf16_f32 v0, v40, v41
	v_pk_max_i16 v64, v0, 0
	v_cvt_pk_bf16_f32 v0, v42, v43
	v_pk_max_i16 v65, v0, 0
	v_cvt_pk_bf16_f32 v0, v44, v45
	v_pk_max_i16 v66, v0, 0
	v_cvt_pk_bf16_f32 v0, v46, v47
	v_pk_max_i16 v67, v0, 0
	v_mfma_f32_32x32x16_bf16 v[72:87], v[132:135], v[164:167], v[72:87]
	v_cvt_f16_f32_e32 v0, v51
	v_bfe_i32 v36, v0, 15, 1
	v_or_b32_e32 v36, 0x8000, v36
	v_xor_b32_e32 v38, v36, v0
	v_add_u32_e32 v0, 0xfffefe00, v190
	v_lshl_add_u64 v[36:37], v[0:1], 1, s[12:13]
	v_lshrrev_b32_e32 v0, 4, v38
	v_and_b32_e32 v0, 0xffc, v0
	global_store_short v[36:37], v38, off
	v_add_u32_e32 v0, v187, v0
	ds_add_u32 v0, v228 offset:29696
	s_waitcnt lgkmcnt(7)
	v_mfma_f32_32x32x16_bf16 v[32:47], v[56:59], v[32:35], 0
	s_waitcnt lgkmcnt(6)
	v_mfma_f32_32x32x16_bf16 v[32:47], v[60:63], v[64:67], v[32:47]
	v_mfma_f32_32x32x16_bf16 v[56:71], v[128:131], v[176:179], 0
	v_cvt_f16_f32_e32 v0, v52
	v_bfe_i32 v191, v0, 15, 1
	v_or_b32_e32 v191, 0x8000, v191
	v_xor_b32_e32 v191, v191, v0
	v_add_u32_e32 v0, 0xffff9f40, v190
	v_lshl_add_u64 v[204:205], v[0:1], 1, s[12:13]
	v_lshrrev_b32_e32 v0, 4, v191
	v_and_b32_e32 v0, 0xffc, v0
	global_store_short v[204:205], v191, off
	v_add_u32_e32 v0, v187, v0
	ds_add_u32 v0, v228 offset:50176
	v_mfma_f32_32x32x16_bf16 v[56:71], v[124:127], v[172:175], v[56:71]
	v_cvt_pk_bf16_f32 v0, v72, v73
	v_pk_max_i16 v72, v0, 0
	v_cvt_pk_bf16_f32 v0, v74, v75
	v_pk_max_i16 v73, v0, 0
	v_cvt_pk_bf16_f32 v0, v76, v77
	v_pk_max_i16 v74, v0, 0
	v_cvt_pk_bf16_f32 v0, v78, v79
	v_pk_max_i16 v75, v0, 0
	v_mfma_f32_32x32x16_bf16 v[56:71], v[120:123], v[168:171], v[56:71]
	ds_read_b128 v[204:207], v203 offset:4096
	ds_read_b128 v[216:219], v203 offset:5120
	v_cvt_pk_bf16_f32 v0, v80, v81
	v_pk_max_i16 v76, v0, 0
	v_cvt_pk_bf16_f32 v0, v82, v83
	v_pk_max_i16 v77, v0, 0
	v_cvt_pk_bf16_f32 v0, v84, v85
	v_pk_max_i16 v78, v0, 0
	v_cvt_pk_bf16_f32 v0, v86, v87
	v_pk_max_i16 v79, v0, 0
	v_mfma_f32_32x32x16_bf16 v[56:71], v[116:119], v[164:167], v[56:71]
	s_waitcnt lgkmcnt(5)
	v_mfma_f32_32x32x16_bf16 v[32:47], v[88:91], v[72:75], v[32:47]
	v_cvt_f16_f32_e32 v0, v53
	v_bfe_i32 v72, v0, 15, 1
	v_or_b32_e32 v72, 0x8000, v72
	v_xor_b32_e32 v74, v72, v0
	v_add_u32_e32 v0, 0xffffbf80, v190
	v_lshl_add_u64 v[72:73], v[0:1], 1, s[12:13]
	v_lshrrev_b32_e32 v0, 4, v74
	v_and_b32_e32 v0, 0xffc, v0
	global_store_short v[72:73], v74, off
	v_add_u32_e32 v0, v187, v0
	ds_add_u32 v0, v228 offset:54272
	s_waitcnt lgkmcnt(5)
	v_mfma_f32_32x32x16_bf16 v[32:47], v[92:95], v[76:79], v[32:47]
	v_mfma_f32_32x32x16_bf16 v[72:87], v[112:115], v[176:179], 0
	v_cvt_f16_f32_e32 v0, v54
	v_bfe_i32 v88, v0, 15, 1
	v_or_b32_e32 v88, 0x8000, v88
	v_xor_b32_e32 v90, v88, v0
	v_add_u32_e32 v0, 0xffffdfc0, v190
	v_lshl_add_u64 v[88:89], v[0:1], 1, s[12:13]
	v_lshrrev_b32_e32 v0, 4, v90
	v_and_b32_e32 v0, 0xffc, v0
	global_store_short v[88:89], v90, off
	v_add_u32_e32 v0, v187, v0
	ds_add_u32 v0, v228 offset:58368
	v_mfma_f32_32x32x16_bf16 v[72:87], v[108:111], v[172:175], v[72:87]
	v_cvt_pk_bf16_f32 v0, v56, v57
	v_pk_max_i16 v56, v0, 0
	v_cvt_pk_bf16_f32 v0, v58, v59
	v_pk_max_i16 v57, v0, 0
	v_cvt_pk_bf16_f32 v0, v60, v61
	v_pk_max_i16 v58, v0, 0
	v_cvt_pk_bf16_f32 v0, v62, v63
	v_pk_max_i16 v59, v0, 0
	v_mfma_f32_32x32x16_bf16 v[72:87], v[104:107], v[168:171], v[72:87]
	v_cvt_pk_bf16_f32 v0, v64, v65
	v_pk_max_i16 v60, v0, 0
	v_cvt_pk_bf16_f32 v0, v66, v67
	v_pk_max_i16 v61, v0, 0
	v_cvt_pk_bf16_f32 v0, v68, v69
	v_pk_max_i16 v62, v0, 0
	v_cvt_pk_bf16_f32 v0, v70, v71
	ds_read_b128 v[64:67], v203 offset:6144
	ds_read_b128 v[68:71], v203 offset:7168
	v_pk_max_i16 v63, v0, 0
	v_mfma_f32_32x32x16_bf16 v[72:87], v[100:103], v[164:167], v[72:87]
	v_cvt_f16_f32_e32 v0, v55
	v_mov_b32_e32 v191, v1
	v_bfe_i32 v88, v0, 15, 1
	v_or_b32_e32 v88, 0x8000, v88
	v_xor_b32_e32 v0, v88, v0
	v_lshl_add_u64 v[88:89], v[190:191], 1, s[12:13]
	global_store_short v[88:89], v0, off
	v_lshrrev_b32_e32 v0, 4, v0
	v_and_b32_e32 v0, 0xffc, v0
	v_add_u32_e32 v0, v187, v0
	ds_add_u32 v0, v228 offset:62464
	s_waitcnt lgkmcnt(6)
	v_mfma_f32_32x32x16_bf16 v[32:47], v[204:207], v[56:59], v[32:47]
	s_waitcnt lgkmcnt(5)
	v_mfma_f32_32x32x16_bf16 v[32:47], v[216:219], v[60:63], v[32:47]
	v_cvt_pk_bf16_f32 v0, v72, v73
	v_pk_max_i16 v56, v0, 0
	v_cvt_pk_bf16_f32 v0, v74, v75
	v_pk_max_i16 v57, v0, 0
	v_cvt_pk_bf16_f32 v0, v76, v77
	v_pk_max_i16 v58, v0, 0
	v_cvt_pk_bf16_f32 v0, v78, v79
	v_pk_max_i16 v59, v0, 0
	v_cvt_pk_bf16_f32 v0, v80, v81
	v_pk_max_i16 v60, v0, 0
	v_cvt_pk_bf16_f32 v0, v82, v83
	v_pk_max_i16 v61, v0, 0
	v_cvt_pk_bf16_f32 v0, v84, v85
	v_pk_max_i16 v62, v0, 0
	v_cvt_pk_bf16_f32 v0, v86, v87
	v_pk_max_i16 v63, v0, 0
	s_waitcnt lgkmcnt(2)
	v_mfma_f32_32x32x16_bf16 v[32:47], v[64:67], v[56:59], v[32:47]
	s_waitcnt lgkmcnt(1)
	v_mfma_f32_32x32x16_bf16 v[32:47], v[68:71], v[60:63], v[32:47]
	s_add_i32 s9, s8, 8
	s_cmp_ge_i32 s9, s28
	v_add_u32_e32 v190, 0x200, v190
	s_mov_b64 s[6:7], 0
	s_cselect_b64 s[26:27], -1, 0

.LBB0_1055:
	s_waitcnt vmcnt(8)
	s_nop 5
	v_cvt_f16_f32_e32 v2, v32
	v_or_b32_e32 v0, v202, v189
	v_add_u32_e32 v0, s4, v0
	v_bfe_i32 v3, v2, 15, 1
	v_or_b32_e32 v3, 0x8000, v3
	v_xor_b32_e32 v4, v3, v2
	v_lshl_add_u64 v[2:3], v[0:1], 1, s[12:13]
	global_store_short v[2:3], v4, off
	v_cvt_f16_f32_e32 v3, v33
	v_lshrrev_b32_e32 v2, 4, v4
	v_and_b32_e32 v2, 0xffc, v2
	v_add_u32_e32 v2, v187, v2
	v_cmp_lt_i16_e32 vcc, -1, v3
	ds_add_u32 v2, v228 offset:17408
	s_nop 0
	v_cndmask_b32_e32 v2, v236, v229, vcc
	v_xor_b32_e32 v4, v2, v3
	v_add_u32_e32 v2, 0x2040, v0
	v_mov_b32_e32 v3, v1
	v_lshl_add_u64 v[2:3], v[2:3], 1, s[12:13]
	global_store_short v[2:3], v4, off
	v_cvt_f16_f32_e32 v3, v34
	v_lshrrev_b32_e32 v2, 4, v4
	v_and_b32_e32 v2, 0xffc, v2
	v_add_u32_e32 v2, v187, v2
	v_cmp_lt_i16_e32 vcc, -1, v3
	ds_add_u32 v2, v228 offset:21504
	s_nop 0
	v_cndmask_b32_e32 v2, v236, v229, vcc
	v_xor_b32_e32 v4, v2, v3
	v_add_u32_e32 v2, 0x4080, v0
	v_mov_b32_e32 v3, v1
	v_lshl_add_u64 v[2:3], v[2:3], 1, s[12:13]
	global_store_short v[2:3], v4, off
	v_cvt_f16_f32_e32 v3, v35
	v_lshrrev_b32_e32 v2, 4, v4
	v_and_b32_e32 v2, 0xffc, v2
	v_add_u32_e32 v2, v187, v2
	v_cmp_lt_i16_e32 vcc, -1, v3
	ds_add_u32 v2, v228 offset:25600
	s_nop 0
	v_cndmask_b32_e32 v2, v236, v229, vcc
	v_xor_b32_e32 v4, v2, v3
	v_add_u32_e32 v2, 0x60c0, v0
	v_mov_b32_e32 v3, v1
	v_lshl_add_u64 v[2:3], v[2:3], 1, s[12:13]
	global_store_short v[2:3], v4, off
	v_cvt_f16_f32_e32 v3, v36
	v_lshrrev_b32_e32 v2, 4, v4
	v_and_b32_e32 v2, 0xffc, v2
	v_add_u32_e32 v2, v187, v2
	v_cmp_lt_i16_e32 vcc, -1, v3
	ds_add_u32 v2, v228 offset:29696
	s_nop 0
	v_cndmask_b32_e32 v2, v236, v229, vcc
	v_xor_b32_e32 v4, v2, v3
	v_add_u32_e32 v2, 0x10200, v0
	v_mov_b32_e32 v3, v1
	v_lshl_add_u64 v[2:3], v[2:3], 1, s[12:13]
	global_store_short v[2:3], v4, off
	v_cvt_f16_f32_e32 v3, v37
	v_lshrrev_b32_e32 v2, 4, v4
	v_and_b32_e32 v2, 0xffc, v2
	v_add_u32_e32 v2, v187, v2
	v_cmp_lt_i16_e32 vcc, -1, v3
	ds_add_u32 v2, v228 offset:50176
	s_nop 0
	v_cndmask_b32_e32 v2, v236, v229, vcc
	v_xor_b32_e32 v4, v2, v3
	v_add_u32_e32 v2, 0x12240, v0
	v_mov_b32_e32 v3, v1
	v_lshl_add_u64 v[2:3], v[2:3], 1, s[12:13]
	global_store_short v[2:3], v4, off
	v_cvt_f16_f32_e32 v3, v38
	v_lshrrev_b32_e32 v2, 4, v4
	v_and_b32_e32 v2, 0xffc, v2
	v_add_u32_e32 v2, v187, v2
	v_cmp_lt_i16_e32 vcc, -1, v3
	ds_add_u32 v2, v228 offset:54272
	s_nop 0
	v_cndmask_b32_e32 v2, v236, v229, vcc
	v_xor_b32_e32 v4, v2, v3
	v_add_u32_e32 v2, 0x14280, v0
	v_mov_b32_e32 v3, v1
	v_lshl_add_u64 v[2:3], v[2:3], 1, s[12:13]
	global_store_short v[2:3], v4, off
	v_cvt_f16_f32_e32 v3, v39
	v_lshrrev_b32_e32 v2, 4, v4
	v_and_b32_e32 v2, 0xffc, v2
	v_add_u32_e32 v2, v187, v2
	v_cmp_lt_i16_e32 vcc, -1, v3
	ds_add_u32 v2, v228 offset:58368
	v_add_u32_e32 v0, 0x162c0, v0
	v_cndmask_b32_e32 v2, v236, v229, vcc
	v_xor_b32_e32 v4, v2, v3
	v_lshl_add_u64 v[2:3], v[0:1], 1, s[12:13]
	v_lshrrev_b32_e32 v0, 4, v4
	v_and_b32_e32 v0, 0xffc, v0
	global_store_short v[2:3], v4, off
	v_add_u32_e32 v0, v187, v0
	ds_add_u32 v0, v228 offset:62464
